# speedup vs baseline: 1.0211x; 1.0027x over previous
_Z7gemm128ILi1ELi96EEv8GemmArgs:
	s_cmp_ge_u32 s2, 0x100
	s_cbranch_scc1 .Lou_exit
	s_load_dwordx4 s[4:7], s[0:1], 0x0
	s_load_dwordx2 s[8:9], s[0:1], 0x20
	s_load_dwordx2 s[10:11], s[0:1], 0x38
	s_load_dwordx2 s[24:25], s[0:1], 0x28
	s_load_dwordx2 s[26:27], s[0:1], 0x40
	s_load_dwordx2 s[28:29], s[0:1], 0x48
	s_and_b32 s12, s2, 7
	s_lshr_b32 s13, s2, 3
	s_lshl_b32 s12, s12, 5
	s_add_u32 s12, s12, s13
	s_and_b32 s13, s12, 3
	s_lshl_b32 s30, s13, 2
	s_lshr_b32 s12, s12, 2
	s_lshl_b32 s12, s12, 7
	s_mul_i32 s13, s13, 0xc0
	v_lshrrev_b32_e32 v1, 6, v0
	v_and_b32_e32 v14, 7, v0
	v_bfe_u32 v15, v0, 4, 3
	v_xor_b32_e32 v14, v14, v15
	v_readfirstlane_b32 s14, v1
	v_lshrrev_b32_e32 v15, 3, v0
	v_mul_u32_u24_e32 v15, 0x600, v15
	v_lshl_add_u32 v2, v14, 4, v15
	s_mov_b32 s22, 0xc000
	v_add_u32_e32 v3, s22, v2
	v_add_u32_e32 v4, s22, v3
	v_add_u32_e32 v5, s22, v4
	v_add_u32_e32 v6, s22, v5
	v_add_u32_e32 v7, s22, v6
	v_and_b32_e32 v14, 15, v0
	v_bfe_u32 v15, v0, 4, 2
	v_lshrrev_b32_e32 v16, 1, v14
	v_xor_b32_e32 v16, v16, v15
	v_lshlrev_b32_e32 v16, 4, v16
	v_bfe_u32 v17, v0, 7, 1
	v_bfe_u32 v18, v0, 6, 1
	v_lshl_add_u32 v19, v17, 6, v14
	v_lshl_add_u32 v8, v19, 7, v16
	v_mul_u32_u24_e32 v19, 0x60, v18
	v_add_u32_e32 v19, v19, v14
	v_lshl_add_u32 v9, v19, 7, v16
	v_add_u32_e32 v9, 0x4000, v9
	v_lshl_add_u32 v19, v17, 6, v14
	v_add_u32_e32 v19, s12, v19
	v_mul_u32_u24_e32 v19, 0xc00, v19
	v_mul_u32_u24_e32 v60, 0x60, v18
	v_lshl_add_u32 v60, v15, 2, v60
	v_add_u32_e32 v60, s13, v60
	v_lshl_add_u32 v56, v60, 2, v19
	s_mov_b32 s22, 0xc000
	v_add_u32_e32 v57, s22, v56
	v_add_u32_e32 v58, s22, v57
	v_add_u32_e32 v59, s22, v58
	s_waitcnt lgkmcnt(0)
	s_mul_i32 s22, s12, 0x600
	s_add_u32 s16, s4, s22
	s_addc_u32 s17, s5, 0
	s_mul_i32 s22, s13, 0x600
	s_add_u32 s18, s6, s22
	s_addc_u32 s19, s7, 0
	s_lshl_b32 s20, s14, 10
	s_mov_b32 s21, 0
	s_add_u32 m0, s20, 0x0
	s_nop 0
	global_load_lds_dwordx4 v2, s[16:17]
	s_add_u32 m0, s20, 0x1000
	s_nop 0
	global_load_lds_dwordx4 v3, s[16:17]
	s_add_u32 m0, s20, 0x2000
	s_nop 0
	global_load_lds_dwordx4 v4, s[16:17]
	s_add_u32 m0, s20, 0x3000
	s_nop 0
	global_load_lds_dwordx4 v5, s[16:17]
	s_add_u32 m0, s20, 0x4000
	s_nop 0
	global_load_lds_dwordx4 v2, s[18:19]
	s_add_u32 m0, s20, 0x5000
	s_nop 0
	global_load_lds_dwordx4 v3, s[18:19]
	s_add_u32 m0, s20, 0x6000
	s_nop 0
	global_load_lds_dwordx4 v4, s[18:19]
	s_add_u32 m0, s20, 0x7000
	s_nop 0
	global_load_lds_dwordx4 v5, s[18:19]
	s_add_u32 m0, s20, 0x8000
	s_nop 0
	global_load_lds_dwordx4 v6, s[18:19]
	s_add_u32 m0, s20, 0x9000
	s_nop 0
	global_load_lds_dwordx4 v7, s[18:19]
	s_add_u32 s16, s16, 0x80
	s_addc_u32 s17, s17, 0
	s_add_u32 s18, s18, 0x80
	s_addc_u32 s19, s19, 0
	s_add_u32 s20, s20, 0xa000
	s_sub_u32 s22, s20, 0x28000
	s_cmp_ge_u32 s20, 0x28000
	s_cselect_b32 s20, s22, s20
	s_add_u32 m0, s20, 0x0
	s_nop 0
	global_load_lds_dwordx4 v2, s[16:17]
	s_add_u32 m0, s20, 0x1000
	s_nop 0
	global_load_lds_dwordx4 v3, s[16:17]
	s_add_u32 m0, s20, 0x2000
	s_nop 0
	global_load_lds_dwordx4 v4, s[16:17]
	s_add_u32 m0, s20, 0x3000
	s_nop 0
	global_load_lds_dwordx4 v5, s[16:17]
	s_add_u32 m0, s20, 0x4000
	s_nop 0
	global_load_lds_dwordx4 v2, s[18:19]
	s_add_u32 m0, s20, 0x5000
	s_nop 0
	global_load_lds_dwordx4 v3, s[18:19]
	s_add_u32 m0, s20, 0x6000
	s_nop 0
	global_load_lds_dwordx4 v4, s[18:19]
	s_add_u32 m0, s20, 0x7000
	s_nop 0
	global_load_lds_dwordx4 v5, s[18:19]
	s_add_u32 m0, s20, 0x8000
	s_nop 0
	global_load_lds_dwordx4 v6, s[18:19]
	s_add_u32 m0, s20, 0x9000
	s_nop 0
	global_load_lds_dwordx4 v7, s[18:19]
	s_add_u32 s16, s16, 0x80
	s_addc_u32 s17, s17, 0
	s_add_u32 s18, s18, 0x80
	s_addc_u32 s19, s19, 0
	s_add_u32 s20, s20, 0xa000
	s_sub_u32 s22, s20, 0x28000
	s_cmp_ge_u32 s20, 0x28000
	s_cselect_b32 s20, s22, s20
	s_add_u32 m0, s20, 0x0
	s_nop 0
	global_load_lds_dwordx4 v2, s[16:17]
	s_add_u32 m0, s20, 0x1000
	s_nop 0
	global_load_lds_dwordx4 v3, s[16:17]
	s_add_u32 m0, s20, 0x2000
	s_nop 0
	global_load_lds_dwordx4 v4, s[16:17]
	s_add_u32 m0, s20, 0x3000
	s_nop 0
	global_load_lds_dwordx4 v5, s[16:17]
	s_add_u32 m0, s20, 0x4000
	s_nop 0
	global_load_lds_dwordx4 v2, s[18:19]
	s_add_u32 m0, s20, 0x5000
	s_nop 0
	global_load_lds_dwordx4 v3, s[18:19]
	s_add_u32 m0, s20, 0x6000
	s_nop 0
	global_load_lds_dwordx4 v4, s[18:19]
	s_add_u32 m0, s20, 0x7000
	s_nop 0
	global_load_lds_dwordx4 v5, s[18:19]
	s_add_u32 m0, s20, 0x8000
	s_nop 0
	global_load_lds_dwordx4 v6, s[18:19]
	s_add_u32 m0, s20, 0x9000
	s_nop 0
	global_load_lds_dwordx4 v7, s[18:19]
	s_add_u32 s16, s16, 0x80
	s_addc_u32 s17, s17, 0
	s_add_u32 s18, s18, 0x80
	s_addc_u32 s19, s19, 0
	s_add_u32 s20, s20, 0xa000
	s_sub_u32 s22, s20, 0x28000
	s_cmp_ge_u32 s20, 0x28000
	s_cselect_b32 s20, s22, s20
	s_add_u32 m0, s20, 0x0
	s_nop 0
	global_load_lds_dwordx4 v2, s[16:17]
	s_add_u32 m0, s20, 0x1000
	s_nop 0
	global_load_lds_dwordx4 v3, s[16:17]
	s_add_u32 m0, s20, 0x2000
	s_nop 0
	global_load_lds_dwordx4 v4, s[16:17]
	s_add_u32 m0, s20, 0x3000
	s_nop 0
	global_load_lds_dwordx4 v5, s[16:17]
	s_add_u32 m0, s20, 0x4000
	s_nop 0
	global_load_lds_dwordx4 v2, s[18:19]
	v_mov_b32_e32 v64, 0
	v_mov_b32_e32 v65, 0
	v_mov_b32_e32 v66, 0
	v_mov_b32_e32 v67, 0
	v_mov_b32_e32 v68, 0
	v_mov_b32_e32 v69, 0
	v_mov_b32_e32 v70, 0
	v_mov_b32_e32 v71, 0
	v_mov_b32_e32 v72, 0
	v_mov_b32_e32 v73, 0
	v_mov_b32_e32 v74, 0
	v_mov_b32_e32 v75, 0
	v_mov_b32_e32 v76, 0
	v_mov_b32_e32 v77, 0
	v_mov_b32_e32 v78, 0
	v_mov_b32_e32 v79, 0
	v_mov_b32_e32 v80, 0
	v_mov_b32_e32 v81, 0
	v_mov_b32_e32 v82, 0
	v_mov_b32_e32 v83, 0
	v_mov_b32_e32 v84, 0
	v_mov_b32_e32 v85, 0
	v_mov_b32_e32 v86, 0
	v_mov_b32_e32 v87, 0
	v_mov_b32_e32 v88, 0
	v_mov_b32_e32 v89, 0
	v_mov_b32_e32 v90, 0
	v_mov_b32_e32 v91, 0
	v_mov_b32_e32 v92, 0
	v_mov_b32_e32 v93, 0
	v_mov_b32_e32 v94, 0
	v_mov_b32_e32 v95, 0
	v_mov_b32_e32 v96, 0
	v_mov_b32_e32 v97, 0
	v_mov_b32_e32 v98, 0
	v_mov_b32_e32 v99, 0
	v_mov_b32_e32 v100, 0
	v_mov_b32_e32 v101, 0
	v_mov_b32_e32 v102, 0
	v_mov_b32_e32 v103, 0
	v_mov_b32_e32 v104, 0
	v_mov_b32_e32 v105, 0
	v_mov_b32_e32 v106, 0
	v_mov_b32_e32 v107, 0
	v_mov_b32_e32 v108, 0
	v_mov_b32_e32 v109, 0
	v_mov_b32_e32 v110, 0
	v_mov_b32_e32 v111, 0
	v_mov_b32_e32 v112, 0
	v_mov_b32_e32 v113, 0
	v_mov_b32_e32 v114, 0
	v_mov_b32_e32 v115, 0
	v_mov_b32_e32 v116, 0
	v_mov_b32_e32 v117, 0
	v_mov_b32_e32 v118, 0
	v_mov_b32_e32 v119, 0
	v_mov_b32_e32 v120, 0
	v_mov_b32_e32 v121, 0
	v_mov_b32_e32 v122, 0
	v_mov_b32_e32 v123, 0
	v_mov_b32_e32 v124, 0
	v_mov_b32_e32 v125, 0
	v_mov_b32_e32 v126, 0
	v_mov_b32_e32 v127, 0
	v_mov_b32_e32 v128, 0
	v_mov_b32_e32 v129, 0
	v_mov_b32_e32 v130, 0
	v_mov_b32_e32 v131, 0
	v_mov_b32_e32 v132, 0
	v_mov_b32_e32 v133, 0
	v_mov_b32_e32 v134, 0
	v_mov_b32_e32 v135, 0
	v_mov_b32_e32 v136, 0
	v_mov_b32_e32 v137, 0
	v_mov_b32_e32 v138, 0
	v_mov_b32_e32 v139, 0
	v_mov_b32_e32 v140, 0
	v_mov_b32_e32 v141, 0
	v_mov_b32_e32 v142, 0
	v_mov_b32_e32 v143, 0
	v_mov_b32_e32 v144, 0
	v_mov_b32_e32 v145, 0
	v_mov_b32_e32 v146, 0
	v_mov_b32_e32 v147, 0
	v_mov_b32_e32 v148, 0
	v_mov_b32_e32 v149, 0
	v_mov_b32_e32 v150, 0
	v_mov_b32_e32 v151, 0
	v_mov_b32_e32 v152, 0
	v_mov_b32_e32 v153, 0
	v_mov_b32_e32 v154, 0
	v_mov_b32_e32 v155, 0
	v_mov_b32_e32 v156, 0
	v_mov_b32_e32 v157, 0
	v_mov_b32_e32 v158, 0
	v_mov_b32_e32 v159, 0
	s_waitcnt vmcnt(25)
	s_barrier
	v_add_u32_e32 v10, s21, v8
	v_add_u32_e32 v12, s21, v9
	v_xor_b32_e32 v11, 64, v10
	v_xor_b32_e32 v13, 64, v12
	s_add_u32 s21, s21, 0xa000
	s_sub_u32 s23, s21, 0x28000
	s_cmp_ge_u32 s21, 0x28000
	s_cselect_b32 s21, s23, s21
	ds_read_b128 v[160:163], v10 offset:0
	ds_read_b128 v[164:167], v10 offset:2048
	ds_read_b128 v[168:171], v10 offset:4096
	ds_read_b128 v[172:175], v10 offset:6144
	ds_read_b128 v[176:179], v12 offset:0
	ds_read_b128 v[180:183], v12 offset:2048
	ds_read_b128 v[184:187], v12 offset:4096
	ds_read_b128 v[188:191], v12 offset:6144
	ds_read_b128 v[192:195], v12 offset:8192
	ds_read_b128 v[196:199], v12 offset:10240
	s_mov_b32 s15, 0
.Lou_loop:
	s_waitcnt lgkmcnt(0)
	v_mfma_f32_16x16x32_bf16 v[64:67], v[176:179], v[160:163], v[64:67]
	ds_read_b128 v[200:203], v11 offset:0
	v_mfma_f32_16x16x32_bf16 v[68:71], v[176:179], v[164:167], v[68:71]
	s_add_u32 m0, s20, 0x5000
	v_mfma_f32_16x16x32_bf16 v[72:75], v[176:179], v[168:171], v[72:75]
	ds_read_b128 v[204:207], v11 offset:2048
	v_mfma_f32_16x16x32_bf16 v[76:79], v[176:179], v[172:175], v[76:79]
	global_load_lds_dwordx4 v3, s[18:19]
	v_mfma_f32_16x16x32_bf16 v[80:83], v[180:183], v[160:163], v[80:83]
	ds_read_b128 v[208:211], v11 offset:4096
	v_mfma_f32_16x16x32_bf16 v[84:87], v[180:183], v[164:167], v[84:87]
	s_add_u32 m0, s20, 0x6000
	v_mfma_f32_16x16x32_bf16 v[88:91], v[180:183], v[168:171], v[88:91]
	ds_read_b128 v[212:215], v11 offset:6144
	v_mfma_f32_16x16x32_bf16 v[92:95], v[180:183], v[172:175], v[92:95]
	global_load_lds_dwordx4 v4, s[18:19]
	v_mfma_f32_16x16x32_bf16 v[96:99], v[184:187], v[160:163], v[96:99]
	ds_read_b128 v[216:219], v13 offset:0
	v_mfma_f32_16x16x32_bf16 v[100:103], v[184:187], v[164:167], v[100:103]
	s_add_u32 m0, s20, 0x7000
	v_mfma_f32_16x16x32_bf16 v[104:107], v[184:187], v[168:171], v[104:107]
	ds_read_b128 v[220:223], v13 offset:2048
	v_mfma_f32_16x16x32_bf16 v[108:111], v[184:187], v[172:175], v[108:111]
	global_load_lds_dwordx4 v5, s[18:19]
	v_mfma_f32_16x16x32_bf16 v[112:115], v[188:191], v[160:163], v[112:115]
	ds_read_b128 v[224:227], v13 offset:4096
	v_mfma_f32_16x16x32_bf16 v[116:119], v[188:191], v[164:167], v[116:119]
	s_add_u32 m0, s20, 0x8000
	v_mfma_f32_16x16x32_bf16 v[120:123], v[188:191], v[168:171], v[120:123]
	ds_read_b128 v[228:231], v13 offset:6144
	v_mfma_f32_16x16x32_bf16 v[124:127], v[188:191], v[172:175], v[124:127]
	global_load_lds_dwordx4 v6, s[18:19]
	v_mfma_f32_16x16x32_bf16 v[128:131], v[192:195], v[160:163], v[128:131]
	ds_read_b128 v[232:235], v13 offset:8192
	v_mfma_f32_16x16x32_bf16 v[132:135], v[192:195], v[164:167], v[132:135]
	s_add_u32 m0, s20, 0x9000
	v_mfma_f32_16x16x32_bf16 v[136:139], v[192:195], v[168:171], v[136:139]
	ds_read_b128 v[236:239], v13 offset:10240
	v_mfma_f32_16x16x32_bf16 v[140:143], v[192:195], v[172:175], v[140:143]
	global_load_lds_dwordx4 v7, s[18:19]
	v_mfma_f32_16x16x32_bf16 v[144:147], v[196:199], v[160:163], v[144:147]
	s_add_u32 s16, s16, 0x80
	s_addc_u32 s17, s17, 0
	s_add_u32 s18, s18, 0x80
	s_addc_u32 s19, s19, 0
	v_mfma_f32_16x16x32_bf16 v[148:151], v[196:199], v[164:167], v[148:151]
	s_add_u32 s20, s20, 0xa000
	s_sub_u32 s22, s20, 0x28000
	s_cmp_ge_u32 s20, 0x28000
	s_cselect_b32 s20, s22, s20
	v_mfma_f32_16x16x32_bf16 v[152:155], v[196:199], v[168:171], v[152:155]
	v_add_u32_e32 v10, s21, v8
	v_add_u32_e32 v12, s21, v9
	v_xor_b32_e32 v11, 64, v10
	v_xor_b32_e32 v13, 64, v12
	v_mfma_f32_16x16x32_bf16 v[156:159], v[196:199], v[172:175], v[156:159]
	s_add_u32 s21, s21, 0xa000
	s_sub_u32 s23, s21, 0x28000
	s_cmp_ge_u32 s21, 0x28000
	s_cselect_b32 s21, s23, s21
	s_waitcnt vmcnt(20) lgkmcnt(0)
	s_barrier
	v_mfma_f32_16x16x32_bf16 v[64:67], v[216:219], v[200:203], v[64:67]
	ds_read_b128 v[160:163], v10 offset:0
	v_mfma_f32_16x16x32_bf16 v[68:71], v[216:219], v[204:207], v[68:71]
	s_add_u32 m0, s20, 0x0
	v_mfma_f32_16x16x32_bf16 v[72:75], v[216:219], v[208:211], v[72:75]
	ds_read_b128 v[164:167], v10 offset:2048
	v_mfma_f32_16x16x32_bf16 v[76:79], v[216:219], v[212:215], v[76:79]
	global_load_lds_dwordx4 v2, s[16:17]
	v_mfma_f32_16x16x32_bf16 v[80:83], v[220:223], v[200:203], v[80:83]
	ds_read_b128 v[168:171], v10 offset:4096
	v_mfma_f32_16x16x32_bf16 v[84:87], v[220:223], v[204:207], v[84:87]
	s_add_u32 m0, s20, 0x1000
	v_mfma_f32_16x16x32_bf16 v[88:91], v[220:223], v[208:211], v[88:91]
	ds_read_b128 v[172:175], v10 offset:6144
	v_mfma_f32_16x16x32_bf16 v[92:95], v[220:223], v[212:215], v[92:95]
	global_load_lds_dwordx4 v3, s[16:17]
	v_mfma_f32_16x16x32_bf16 v[96:99], v[224:227], v[200:203], v[96:99]
	ds_read_b128 v[176:179], v12 offset:0
	v_mfma_f32_16x16x32_bf16 v[100:103], v[224:227], v[204:207], v[100:103]
	s_add_u32 m0, s20, 0x2000
	v_mfma_f32_16x16x32_bf16 v[104:107], v[224:227], v[208:211], v[104:107]
	ds_read_b128 v[180:183], v12 offset:2048
	v_mfma_f32_16x16x32_bf16 v[108:111], v[224:227], v[212:215], v[108:111]
	global_load_lds_dwordx4 v4, s[16:17]
	v_mfma_f32_16x16x32_bf16 v[112:115], v[228:231], v[200:203], v[112:115]
	ds_read_b128 v[184:187], v12 offset:4096
	v_mfma_f32_16x16x32_bf16 v[116:119], v[228:231], v[204:207], v[116:119]
	s_add_u32 m0, s20, 0x3000
	v_mfma_f32_16x16x32_bf16 v[120:123], v[228:231], v[208:211], v[120:123]
	ds_read_b128 v[188:191], v12 offset:6144
	v_mfma_f32_16x16x32_bf16 v[124:127], v[228:231], v[212:215], v[124:127]
	global_load_lds_dwordx4 v5, s[16:17]
	v_mfma_f32_16x16x32_bf16 v[128:131], v[232:235], v[200:203], v[128:131]
	ds_read_b128 v[192:195], v12 offset:8192
	v_mfma_f32_16x16x32_bf16 v[132:135], v[232:235], v[204:207], v[132:135]
	s_add_u32 m0, s20, 0x4000
	v_mfma_f32_16x16x32_bf16 v[136:139], v[232:235], v[208:211], v[136:139]
	ds_read_b128 v[196:199], v12 offset:10240
	v_mfma_f32_16x16x32_bf16 v[140:143], v[232:235], v[212:215], v[140:143]
	global_load_lds_dwordx4 v2, s[18:19]
	v_mfma_f32_16x16x32_bf16 v[144:147], v[236:239], v[200:203], v[144:147]
	v_mfma_f32_16x16x32_bf16 v[148:151], v[236:239], v[204:207], v[148:151]
	v_mfma_f32_16x16x32_bf16 v[152:155], v[236:239], v[208:211], v[152:155]
	v_mfma_f32_16x16x32_bf16 v[156:159], v[236:239], v[212:215], v[156:159]
	s_add_u32 s15, s15, 1
	s_cmp_lt_u32 s15, 8
	s_cbranch_scc1 .Lou_loop
	s_waitcnt lgkmcnt(0)
	v_mfma_f32_16x16x32_bf16 v[64:67], v[176:179], v[160:163], v[64:67]
	ds_read_b128 v[200:203], v11 offset:0
	v_mfma_f32_16x16x32_bf16 v[68:71], v[176:179], v[164:167], v[68:71]
	s_add_u32 m0, s20, 0x5000
	v_mfma_f32_16x16x32_bf16 v[72:75], v[176:179], v[168:171], v[72:75]
	ds_read_b128 v[204:207], v11 offset:2048
	v_mfma_f32_16x16x32_bf16 v[76:79], v[176:179], v[172:175], v[76:79]
	global_load_lds_dwordx4 v3, s[18:19]
	v_mfma_f32_16x16x32_bf16 v[80:83], v[180:183], v[160:163], v[80:83]
	ds_read_b128 v[208:211], v11 offset:4096
	v_mfma_f32_16x16x32_bf16 v[84:87], v[180:183], v[164:167], v[84:87]
	s_add_u32 m0, s20, 0x6000
	v_mfma_f32_16x16x32_bf16 v[88:91], v[180:183], v[168:171], v[88:91]
	ds_read_b128 v[212:215], v11 offset:6144
	v_mfma_f32_16x16x32_bf16 v[92:95], v[180:183], v[172:175], v[92:95]
	global_load_lds_dwordx4 v4, s[18:19]
	v_mfma_f32_16x16x32_bf16 v[96:99], v[184:187], v[160:163], v[96:99]
	ds_read_b128 v[216:219], v13 offset:0
	v_mfma_f32_16x16x32_bf16 v[100:103], v[184:187], v[164:167], v[100:103]
	s_add_u32 m0, s20, 0x7000
	v_mfma_f32_16x16x32_bf16 v[104:107], v[184:187], v[168:171], v[104:107]
	ds_read_b128 v[220:223], v13 offset:2048
	v_mfma_f32_16x16x32_bf16 v[108:111], v[184:187], v[172:175], v[108:111]
	global_load_lds_dwordx4 v5, s[18:19]
	v_mfma_f32_16x16x32_bf16 v[112:115], v[188:191], v[160:163], v[112:115]
	ds_read_b128 v[224:227], v13 offset:4096
	v_mfma_f32_16x16x32_bf16 v[116:119], v[188:191], v[164:167], v[116:119]
	s_add_u32 m0, s20, 0x8000
	v_mfma_f32_16x16x32_bf16 v[120:123], v[188:191], v[168:171], v[120:123]
	ds_read_b128 v[228:231], v13 offset:6144
	v_mfma_f32_16x16x32_bf16 v[124:127], v[188:191], v[172:175], v[124:127]
	global_load_lds_dwordx4 v6, s[18:19]
	v_mfma_f32_16x16x32_bf16 v[128:131], v[192:195], v[160:163], v[128:131]
	ds_read_b128 v[232:235], v13 offset:8192
	v_mfma_f32_16x16x32_bf16 v[132:135], v[192:195], v[164:167], v[132:135]
	s_add_u32 m0, s20, 0x9000
	v_mfma_f32_16x16x32_bf16 v[136:139], v[192:195], v[168:171], v[136:139]
	ds_read_b128 v[236:239], v13 offset:10240
	v_mfma_f32_16x16x32_bf16 v[140:143], v[192:195], v[172:175], v[140:143]
	global_load_lds_dwordx4 v7, s[18:19]
	v_mfma_f32_16x16x32_bf16 v[144:147], v[196:199], v[160:163], v[144:147]
	s_add_u32 s16, s16, 0x80
	s_addc_u32 s17, s17, 0
	s_add_u32 s18, s18, 0x80
	s_addc_u32 s19, s19, 0
	v_mfma_f32_16x16x32_bf16 v[148:151], v[196:199], v[164:167], v[148:151]
	s_add_u32 s20, s20, 0xa000
	s_sub_u32 s22, s20, 0x28000
	s_cmp_ge_u32 s20, 0x28000
	s_cselect_b32 s20, s22, s20
	v_mfma_f32_16x16x32_bf16 v[152:155], v[196:199], v[168:171], v[152:155]
	v_add_u32_e32 v10, s21, v8
	v_add_u32_e32 v12, s21, v9
	v_xor_b32_e32 v11, 64, v10
	v_xor_b32_e32 v13, 64, v12
	v_mfma_f32_16x16x32_bf16 v[156:159], v[196:199], v[172:175], v[156:159]
	s_add_u32 s21, s21, 0xa000
	s_sub_u32 s23, s21, 0x28000
	s_cmp_ge_u32 s21, 0x28000
	s_cselect_b32 s21, s23, s21
	s_waitcnt vmcnt(20) lgkmcnt(0)
	s_barrier
	v_mfma_f32_16x16x32_bf16 v[64:67], v[216:219], v[200:203], v[64:67]
	ds_read_b128 v[160:163], v10 offset:0
	v_mfma_f32_16x16x32_bf16 v[68:71], v[216:219], v[204:207], v[68:71]
	ds_read_b128 v[164:167], v10 offset:2048
	v_mfma_f32_16x16x32_bf16 v[72:75], v[216:219], v[208:211], v[72:75]
	ds_read_b128 v[168:171], v10 offset:4096
	v_mfma_f32_16x16x32_bf16 v[76:79], v[216:219], v[212:215], v[76:79]
	ds_read_b128 v[172:175], v10 offset:6144
	v_mfma_f32_16x16x32_bf16 v[80:83], v[220:223], v[200:203], v[80:83]
	ds_read_b128 v[176:179], v12 offset:0
	v_mfma_f32_16x16x32_bf16 v[84:87], v[220:223], v[204:207], v[84:87]
	ds_read_b128 v[180:183], v12 offset:2048
	v_mfma_f32_16x16x32_bf16 v[88:91], v[220:223], v[208:211], v[88:91]
	ds_read_b128 v[184:187], v12 offset:4096
	v_mfma_f32_16x16x32_bf16 v[92:95], v[220:223], v[212:215], v[92:95]
	ds_read_b128 v[188:191], v12 offset:6144
	v_mfma_f32_16x16x32_bf16 v[96:99], v[224:227], v[200:203], v[96:99]
	ds_read_b128 v[192:195], v12 offset:8192
	v_mfma_f32_16x16x32_bf16 v[100:103], v[224:227], v[204:207], v[100:103]
	ds_read_b128 v[196:199], v12 offset:10240
	v_mfma_f32_16x16x32_bf16 v[104:107], v[224:227], v[208:211], v[104:107]
	v_mfma_f32_16x16x32_bf16 v[108:111], v[224:227], v[212:215], v[108:111]
	v_mfma_f32_16x16x32_bf16 v[112:115], v[228:231], v[200:203], v[112:115]
	v_mfma_f32_16x16x32_bf16 v[116:119], v[228:231], v[204:207], v[116:119]
	v_mfma_f32_16x16x32_bf16 v[120:123], v[228:231], v[208:211], v[120:123]
	v_mfma_f32_16x16x32_bf16 v[124:127], v[228:231], v[212:215], v[124:127]
	v_mfma_f32_16x16x32_bf16 v[128:131], v[232:235], v[200:203], v[128:131]
	v_mfma_f32_16x16x32_bf16 v[132:135], v[232:235], v[204:207], v[132:135]
	v_mfma_f32_16x16x32_bf16 v[136:139], v[232:235], v[208:211], v[136:139]
	v_mfma_f32_16x16x32_bf16 v[140:143], v[232:235], v[212:215], v[140:143]
	v_mfma_f32_16x16x32_bf16 v[144:147], v[236:239], v[200:203], v[144:147]
	v_mfma_f32_16x16x32_bf16 v[148:151], v[236:239], v[204:207], v[148:151]
	v_mfma_f32_16x16x32_bf16 v[152:155], v[236:239], v[208:211], v[152:155]
	v_mfma_f32_16x16x32_bf16 v[156:159], v[236:239], v[212:215], v[156:159]
	s_waitcnt lgkmcnt(0)
	v_mfma_f32_16x16x32_bf16 v[64:67], v[176:179], v[160:163], v[64:67]
	ds_read_b128 v[200:203], v11 offset:0
	v_mfma_f32_16x16x32_bf16 v[68:71], v[176:179], v[164:167], v[68:71]
	ds_read_b128 v[204:207], v11 offset:2048
	v_mfma_f32_16x16x32_bf16 v[72:75], v[176:179], v[168:171], v[72:75]
	ds_read_b128 v[208:211], v11 offset:4096
	v_mfma_f32_16x16x32_bf16 v[76:79], v[176:179], v[172:175], v[76:79]
	ds_read_b128 v[212:215], v11 offset:6144
	v_mfma_f32_16x16x32_bf16 v[80:83], v[180:183], v[160:163], v[80:83]
	ds_read_b128 v[216:219], v13 offset:0
	v_mfma_f32_16x16x32_bf16 v[84:87], v[180:183], v[164:167], v[84:87]
	ds_read_b128 v[220:223], v13 offset:2048
	v_mfma_f32_16x16x32_bf16 v[88:91], v[180:183], v[168:171], v[88:91]
	ds_read_b128 v[224:227], v13 offset:4096
	v_mfma_f32_16x16x32_bf16 v[92:95], v[180:183], v[172:175], v[92:95]
	ds_read_b128 v[228:231], v13 offset:6144
	v_mfma_f32_16x16x32_bf16 v[96:99], v[184:187], v[160:163], v[96:99]
	ds_read_b128 v[232:235], v13 offset:8192
	v_mfma_f32_16x16x32_bf16 v[100:103], v[184:187], v[164:167], v[100:103]
	ds_read_b128 v[236:239], v13 offset:10240
	v_mfma_f32_16x16x32_bf16 v[104:107], v[184:187], v[168:171], v[104:107]
	v_mfma_f32_16x16x32_bf16 v[108:111], v[184:187], v[172:175], v[108:111]
	v_mfma_f32_16x16x32_bf16 v[112:115], v[188:191], v[160:163], v[112:115]
	v_mfma_f32_16x16x32_bf16 v[116:119], v[188:191], v[164:167], v[116:119]
	v_mfma_f32_16x16x32_bf16 v[120:123], v[188:191], v[168:171], v[120:123]
	v_mfma_f32_16x16x32_bf16 v[124:127], v[188:191], v[172:175], v[124:127]
	v_mfma_f32_16x16x32_bf16 v[128:131], v[192:195], v[160:163], v[128:131]
	v_mfma_f32_16x16x32_bf16 v[132:135], v[192:195], v[164:167], v[132:135]
	v_mfma_f32_16x16x32_bf16 v[136:139], v[192:195], v[168:171], v[136:139]
	v_mfma_f32_16x16x32_bf16 v[140:143], v[192:195], v[172:175], v[140:143]
	v_mfma_f32_16x16x32_bf16 v[144:147], v[196:199], v[160:163], v[144:147]
	v_add_u32_e32 v10, s21, v8
	v_add_u32_e32 v12, s21, v9
	v_xor_b32_e32 v11, 64, v10
	v_xor_b32_e32 v13, 64, v12
	v_mfma_f32_16x16x32_bf16 v[148:151], v[196:199], v[164:167], v[148:151]
	s_add_u32 s21, s21, 0xa000
	s_sub_u32 s23, s21, 0x28000
	s_cmp_ge_u32 s21, 0x28000
	s_cselect_b32 s21, s23, s21
	v_mfma_f32_16x16x32_bf16 v[152:155], v[196:199], v[168:171], v[152:155]
	v_mfma_f32_16x16x32_bf16 v[156:159], v[196:199], v[172:175], v[156:159]
	s_waitcnt vmcnt(10) lgkmcnt(0)
	s_barrier
	v_mfma_f32_16x16x32_bf16 v[64:67], v[216:219], v[200:203], v[64:67]
	ds_read_b128 v[160:163], v10 offset:0
	v_mfma_f32_16x16x32_bf16 v[68:71], v[216:219], v[204:207], v[68:71]
	ds_read_b128 v[164:167], v10 offset:2048
	v_mfma_f32_16x16x32_bf16 v[72:75], v[216:219], v[208:211], v[72:75]
	ds_read_b128 v[168:171], v10 offset:4096
	v_mfma_f32_16x16x32_bf16 v[76:79], v[216:219], v[212:215], v[76:79]
	ds_read_b128 v[172:175], v10 offset:6144
	v_mfma_f32_16x16x32_bf16 v[80:83], v[220:223], v[200:203], v[80:83]
	ds_read_b128 v[176:179], v12 offset:0
	v_mfma_f32_16x16x32_bf16 v[84:87], v[220:223], v[204:207], v[84:87]
	ds_read_b128 v[180:183], v12 offset:2048
	v_mfma_f32_16x16x32_bf16 v[88:91], v[220:223], v[208:211], v[88:91]
	ds_read_b128 v[184:187], v12 offset:4096
	v_mfma_f32_16x16x32_bf16 v[92:95], v[220:223], v[212:215], v[92:95]
	ds_read_b128 v[188:191], v12 offset:6144
	v_mfma_f32_16x16x32_bf16 v[96:99], v[224:227], v[200:203], v[96:99]
	ds_read_b128 v[192:195], v12 offset:8192
	v_mfma_f32_16x16x32_bf16 v[100:103], v[224:227], v[204:207], v[100:103]
	ds_read_b128 v[196:199], v12 offset:10240
	v_mfma_f32_16x16x32_bf16 v[104:107], v[224:227], v[208:211], v[104:107]
	v_mfma_f32_16x16x32_bf16 v[108:111], v[224:227], v[212:215], v[108:111]
	v_mfma_f32_16x16x32_bf16 v[112:115], v[228:231], v[200:203], v[112:115]
	v_mfma_f32_16x16x32_bf16 v[116:119], v[228:231], v[204:207], v[116:119]
	v_mfma_f32_16x16x32_bf16 v[120:123], v[228:231], v[208:211], v[120:123]
	v_mfma_f32_16x16x32_bf16 v[124:127], v[228:231], v[212:215], v[124:127]
	v_mfma_f32_16x16x32_bf16 v[128:131], v[232:235], v[200:203], v[128:131]
	v_mfma_f32_16x16x32_bf16 v[132:135], v[232:235], v[204:207], v[132:135]
	v_mfma_f32_16x16x32_bf16 v[136:139], v[232:235], v[208:211], v[136:139]
	v_mfma_f32_16x16x32_bf16 v[140:143], v[232:235], v[212:215], v[140:143]
	v_mfma_f32_16x16x32_bf16 v[144:147], v[236:239], v[200:203], v[144:147]
	v_mfma_f32_16x16x32_bf16 v[148:151], v[236:239], v[204:207], v[148:151]
	v_mfma_f32_16x16x32_bf16 v[152:155], v[236:239], v[208:211], v[152:155]
	v_mfma_f32_16x16x32_bf16 v[156:159], v[236:239], v[212:215], v[156:159]
	s_waitcnt lgkmcnt(0)
	v_mfma_f32_16x16x32_bf16 v[64:67], v[176:179], v[160:163], v[64:67]
	ds_read_b128 v[200:203], v11 offset:0
	v_mfma_f32_16x16x32_bf16 v[68:71], v[176:179], v[164:167], v[68:71]
	ds_read_b128 v[204:207], v11 offset:2048
	v_mfma_f32_16x16x32_bf16 v[72:75], v[176:179], v[168:171], v[72:75]
	ds_read_b128 v[208:211], v11 offset:4096
	v_mfma_f32_16x16x32_bf16 v[76:79], v[176:179], v[172:175], v[76:79]
	ds_read_b128 v[212:215], v11 offset:6144
	v_mfma_f32_16x16x32_bf16 v[80:83], v[180:183], v[160:163], v[80:83]
	ds_read_b128 v[216:219], v13 offset:0
	v_mfma_f32_16x16x32_bf16 v[84:87], v[180:183], v[164:167], v[84:87]
	ds_read_b128 v[220:223], v13 offset:2048
	v_mfma_f32_16x16x32_bf16 v[88:91], v[180:183], v[168:171], v[88:91]
	ds_read_b128 v[224:227], v13 offset:4096
	v_mfma_f32_16x16x32_bf16 v[92:95], v[180:183], v[172:175], v[92:95]
	ds_read_b128 v[228:231], v13 offset:6144
	v_mfma_f32_16x16x32_bf16 v[96:99], v[184:187], v[160:163], v[96:99]
	ds_read_b128 v[232:235], v13 offset:8192
	v_mfma_f32_16x16x32_bf16 v[100:103], v[184:187], v[164:167], v[100:103]
	ds_read_b128 v[236:239], v13 offset:10240
	v_mfma_f32_16x16x32_bf16 v[104:107], v[184:187], v[168:171], v[104:107]
	v_mfma_f32_16x16x32_bf16 v[108:111], v[184:187], v[172:175], v[108:111]
	v_mfma_f32_16x16x32_bf16 v[112:115], v[188:191], v[160:163], v[112:115]
	v_mfma_f32_16x16x32_bf16 v[116:119], v[188:191], v[164:167], v[116:119]
	v_mfma_f32_16x16x32_bf16 v[120:123], v[188:191], v[168:171], v[120:123]
	v_mfma_f32_16x16x32_bf16 v[124:127], v[188:191], v[172:175], v[124:127]
	v_mfma_f32_16x16x32_bf16 v[128:131], v[192:195], v[160:163], v[128:131]
	v_mfma_f32_16x16x32_bf16 v[132:135], v[192:195], v[164:167], v[132:135]
	v_mfma_f32_16x16x32_bf16 v[136:139], v[192:195], v[168:171], v[136:139]
	v_mfma_f32_16x16x32_bf16 v[140:143], v[192:195], v[172:175], v[140:143]
	v_mfma_f32_16x16x32_bf16 v[144:147], v[196:199], v[160:163], v[144:147]
	v_add_u32_e32 v10, s21, v8
	v_add_u32_e32 v12, s21, v9
	v_xor_b32_e32 v11, 64, v10
	v_xor_b32_e32 v13, 64, v12
	v_mfma_f32_16x16x32_bf16 v[148:151], v[196:199], v[164:167], v[148:151]
	s_add_u32 s21, s21, 0xa000
	s_sub_u32 s23, s21, 0x28000
	s_cmp_ge_u32 s21, 0x28000
	s_cselect_b32 s21, s23, s21
	v_mfma_f32_16x16x32_bf16 v[152:155], v[196:199], v[168:171], v[152:155]
	v_mfma_f32_16x16x32_bf16 v[156:159], v[196:199], v[172:175], v[156:159]
	s_waitcnt vmcnt(0) lgkmcnt(0)
	s_barrier
	v_mfma_f32_16x16x32_bf16 v[64:67], v[216:219], v[200:203], v[64:67]
	ds_read_b128 v[160:163], v10 offset:0
	v_mfma_f32_16x16x32_bf16 v[68:71], v[216:219], v[204:207], v[68:71]
	global_load_dwordx4 v[16:19], v56, s[8:9] offset:0
	v_mfma_f32_16x16x32_bf16 v[72:75], v[216:219], v[208:211], v[72:75]
	ds_read_b128 v[164:167], v10 offset:2048
	v_mfma_f32_16x16x32_bf16 v[76:79], v[216:219], v[212:215], v[76:79]
	global_load_dwordx4 v[20:23], v57, s[8:9] offset:0
	v_mfma_f32_16x16x32_bf16 v[80:83], v[220:223], v[200:203], v[80:83]
	ds_read_b128 v[168:171], v10 offset:4096
	v_mfma_f32_16x16x32_bf16 v[84:87], v[220:223], v[204:207], v[84:87]
	global_load_dwordx4 v[24:27], v58, s[8:9] offset:0
	v_mfma_f32_16x16x32_bf16 v[88:91], v[220:223], v[208:211], v[88:91]
	ds_read_b128 v[172:175], v10 offset:6144
	v_mfma_f32_16x16x32_bf16 v[92:95], v[220:223], v[212:215], v[92:95]
	global_load_dwordx4 v[28:31], v59, s[8:9] offset:0
	v_mfma_f32_16x16x32_bf16 v[96:99], v[224:227], v[200:203], v[96:99]
	ds_read_b128 v[176:179], v12 offset:0
	v_mfma_f32_16x16x32_bf16 v[100:103], v[224:227], v[204:207], v[100:103]
	global_load_dwordx4 v[32:35], v56, s[8:9] offset:64
	v_mfma_f32_16x16x32_bf16 v[104:107], v[224:227], v[208:211], v[104:107]
	ds_read_b128 v[180:183], v12 offset:2048
	v_mfma_f32_16x16x32_bf16 v[108:111], v[224:227], v[212:215], v[108:111]
	global_load_dwordx4 v[36:39], v57, s[8:9] offset:64
	v_mfma_f32_16x16x32_bf16 v[112:115], v[228:231], v[200:203], v[112:115]
	ds_read_b128 v[184:187], v12 offset:4096
	v_mfma_f32_16x16x32_bf16 v[116:119], v[228:231], v[204:207], v[116:119]
	global_load_dwordx4 v[40:43], v58, s[8:9] offset:64
	v_mfma_f32_16x16x32_bf16 v[120:123], v[228:231], v[208:211], v[120:123]
	ds_read_b128 v[188:191], v12 offset:6144
	v_mfma_f32_16x16x32_bf16 v[124:127], v[228:231], v[212:215], v[124:127]
	global_load_dwordx4 v[44:47], v59, s[8:9] offset:64
	v_mfma_f32_16x16x32_bf16 v[128:131], v[232:235], v[200:203], v[128:131]
	ds_read_b128 v[192:195], v12 offset:8192
	v_mfma_f32_16x16x32_bf16 v[132:135], v[232:235], v[204:207], v[132:135]
	global_load_dwordx4 v[48:51], v56, s[8:9] offset:128
	v_mfma_f32_16x16x32_bf16 v[136:139], v[232:235], v[208:211], v[136:139]
	ds_read_b128 v[196:199], v12 offset:10240
	v_mfma_f32_16x16x32_bf16 v[140:143], v[232:235], v[212:215], v[140:143]
	global_load_dwordx4 v[52:55], v57, s[8:9] offset:128
	v_mfma_f32_16x16x32_bf16 v[144:147], v[236:239], v[200:203], v[144:147]
	global_load_dwordx4 v[240:243], v58, s[8:9] offset:128
	v_mfma_f32_16x16x32_bf16 v[148:151], v[236:239], v[204:207], v[148:151]
	global_load_dwordx4 v[244:247], v59, s[8:9] offset:128
	v_mfma_f32_16x16x32_bf16 v[152:155], v[236:239], v[208:211], v[152:155]
	global_load_dwordx4 v[248:251], v56, s[8:9] offset:192
	v_mfma_f32_16x16x32_bf16 v[156:159], v[236:239], v[212:215], v[156:159]
	global_load_dwordx4 v[252:255], v57, s[8:9] offset:192
	s_waitcnt lgkmcnt(0)
	v_mfma_f32_16x16x32_bf16 v[64:67], v[176:179], v[160:163], v[64:67]
	ds_read_b128 v[200:203], v11 offset:0
	v_mfma_f32_16x16x32_bf16 v[68:71], v[176:179], v[164:167], v[68:71]
	ds_read_b128 v[204:207], v11 offset:2048
	v_mfma_f32_16x16x32_bf16 v[72:75], v[176:179], v[168:171], v[72:75]
	ds_read_b128 v[208:211], v11 offset:4096
	v_mfma_f32_16x16x32_bf16 v[76:79], v[176:179], v[172:175], v[76:79]
	ds_read_b128 v[212:215], v11 offset:6144
	v_mfma_f32_16x16x32_bf16 v[80:83], v[180:183], v[160:163], v[80:83]
	ds_read_b128 v[216:219], v13 offset:0
	v_mfma_f32_16x16x32_bf16 v[84:87], v[180:183], v[164:167], v[84:87]
	ds_read_b128 v[220:223], v13 offset:2048
	v_mfma_f32_16x16x32_bf16 v[88:91], v[180:183], v[168:171], v[88:91]
	ds_read_b128 v[224:227], v13 offset:4096
	v_mfma_f32_16x16x32_bf16 v[92:95], v[180:183], v[172:175], v[92:95]
	ds_read_b128 v[228:231], v13 offset:6144
	v_mfma_f32_16x16x32_bf16 v[96:99], v[184:187], v[160:163], v[96:99]
	ds_read_b128 v[232:235], v13 offset:8192
	v_mfma_f32_16x16x32_bf16 v[100:103], v[184:187], v[164:167], v[100:103]
	ds_read_b128 v[236:239], v13 offset:10240
	v_mfma_f32_16x16x32_bf16 v[104:107], v[184:187], v[168:171], v[104:107]
	v_mfma_f32_16x16x32_bf16 v[108:111], v[184:187], v[172:175], v[108:111]
	v_mfma_f32_16x16x32_bf16 v[112:115], v[188:191], v[160:163], v[112:115]
	v_mfma_f32_16x16x32_bf16 v[116:119], v[188:191], v[164:167], v[116:119]
	v_mfma_f32_16x16x32_bf16 v[120:123], v[188:191], v[168:171], v[120:123]
	v_mfma_f32_16x16x32_bf16 v[124:127], v[188:191], v[172:175], v[124:127]
	v_mfma_f32_16x16x32_bf16 v[128:131], v[192:195], v[160:163], v[128:131]
	v_mfma_f32_16x16x32_bf16 v[132:135], v[192:195], v[164:167], v[132:135]
	v_mfma_f32_16x16x32_bf16 v[136:139], v[192:195], v[168:171], v[136:139]
	v_mfma_f32_16x16x32_bf16 v[140:143], v[192:195], v[172:175], v[140:143]
	v_mfma_f32_16x16x32_bf16 v[144:147], v[196:199], v[160:163], v[144:147]
	v_mfma_f32_16x16x32_bf16 v[148:151], v[196:199], v[164:167], v[148:151]
	v_mfma_f32_16x16x32_bf16 v[152:155], v[196:199], v[168:171], v[152:155]
	v_mfma_f32_16x16x32_bf16 v[156:159], v[196:199], v[172:175], v[156:159]
	s_waitcnt lgkmcnt(0)
	v_mfma_f32_16x16x32_bf16 v[64:67], v[216:219], v[200:203], v[64:67]
	v_mfma_f32_16x16x32_bf16 v[68:71], v[216:219], v[204:207], v[68:71]
	global_load_dwordx4 v[160:163], v58, s[8:9] offset:192
	v_mfma_f32_16x16x32_bf16 v[72:75], v[216:219], v[208:211], v[72:75]
	v_mfma_f32_16x16x32_bf16 v[76:79], v[216:219], v[212:215], v[76:79]
	global_load_dwordx4 v[164:167], v59, s[8:9] offset:192
	v_mfma_f32_16x16x32_bf16 v[80:83], v[220:223], v[200:203], v[80:83]
	v_mfma_f32_16x16x32_bf16 v[84:87], v[220:223], v[204:207], v[84:87]
	global_load_dwordx4 v[168:171], v56, s[8:9] offset:256
	v_mfma_f32_16x16x32_bf16 v[88:91], v[220:223], v[208:211], v[88:91]
	v_mfma_f32_16x16x32_bf16 v[92:95], v[220:223], v[212:215], v[92:95]
	global_load_dwordx4 v[172:175], v57, s[8:9] offset:256
	v_mfma_f32_16x16x32_bf16 v[96:99], v[224:227], v[200:203], v[96:99]
	v_mfma_f32_16x16x32_bf16 v[100:103], v[224:227], v[204:207], v[100:103]
	global_load_dwordx4 v[176:179], v58, s[8:9] offset:256
	v_mfma_f32_16x16x32_bf16 v[104:107], v[224:227], v[208:211], v[104:107]
	v_mfma_f32_16x16x32_bf16 v[108:111], v[224:227], v[212:215], v[108:111]
	global_load_dwordx4 v[180:183], v59, s[8:9] offset:256
	v_mfma_f32_16x16x32_bf16 v[112:115], v[228:231], v[200:203], v[112:115]
	v_mfma_f32_16x16x32_bf16 v[116:119], v[228:231], v[204:207], v[116:119]
	global_load_dwordx4 v[184:187], v56, s[8:9] offset:320
	v_mfma_f32_16x16x32_bf16 v[120:123], v[228:231], v[208:211], v[120:123]
	v_mfma_f32_16x16x32_bf16 v[124:127], v[228:231], v[212:215], v[124:127]
	global_load_dwordx4 v[188:191], v57, s[8:9] offset:320
	v_mfma_f32_16x16x32_bf16 v[128:131], v[232:235], v[200:203], v[128:131]
	v_mfma_f32_16x16x32_bf16 v[132:135], v[232:235], v[204:207], v[132:135]
	global_load_dwordx4 v[192:195], v58, s[8:9] offset:320
	v_mfma_f32_16x16x32_bf16 v[136:139], v[232:235], v[208:211], v[136:139]
	v_mfma_f32_16x16x32_bf16 v[140:143], v[232:235], v[212:215], v[140:143]
	global_load_dwordx4 v[196:199], v59, s[8:9] offset:320
	v_mfma_f32_16x16x32_bf16 v[144:147], v[236:239], v[200:203], v[144:147]
	v_mfma_f32_16x16x32_bf16 v[148:151], v[236:239], v[204:207], v[148:151]
	v_mfma_f32_16x16x32_bf16 v[152:155], v[236:239], v[208:211], v[152:155]
	v_mfma_f32_16x16x32_bf16 v[156:159], v[236:239], v[212:215], v[156:159]
	v_and_b32_e32 v12, 63, v0
	v_cmp_gt_u32_e32 vcc, 16, v12
	v_xor_b32_e32 v13, 16, v12
	v_lshlrev_b32_e32 v13, 2, v13
	v_xor_b32_e32 v12, 32, v12
	v_lshlrev_b32_e32 v12, 2, v12
	v_bfe_u32 v14, v0, 6, 1
	v_mul_u32_u24_e32 v14, 0x60, v14
	v_bfe_u32 v15, v0, 4, 2
	v_lshl_add_u32 v14, v15, 2, v14
	v_add_u32_e32 v14, s13, v14
	v_lshlrev_b32_e32 v14, 2, v14
	global_load_dwordx4 v[200:203], v14, s[24:25]
	global_load_dwordx4 v[204:207], v14, s[24:25] offset:64
	global_load_dwordx4 v[208:211], v14, s[24:25] offset:128
	global_load_dwordx4 v[212:215], v14, s[24:25] offset:192
	global_load_dwordx4 v[216:219], v14, s[24:25] offset:256
	global_load_dwordx4 v[220:223], v14, s[24:25] offset:320
	v_lshrrev_b32_e32 v60, 1, v56
	v_lshrrev_b32_e32 v61, 1, v57
	v_lshrrev_b32_e32 v62, 1, v58
	v_lshrrev_b32_e32 v63, 1, v59
	v_bfe_u32 v8, v0, 7, 1
	v_and_b32_e32 v9, 15, v0
	v_lshl_add_u32 v8, v8, 6, v9
	v_add_u32_e32 v8, s12, v8
	v_lshlrev_b32_e32 v8, 6, v8
	v_bfe_u32 v9, v0, 6, 1
	v_lshlrev_b32_e32 v9, 1, v9
	v_add_u32_e32 v9, s30, v9
	v_lshl_add_u32 v8, v9, 2, v8
	v_add_u32_e32 v9, 0x400, v8
	v_add_u32_e32 v10, 0x400, v9
	v_add_u32_e32 v11, 0x400, v10
	s_waitcnt vmcnt(0)
	v_pk_add_f32 v[64:65], v[64:65], v[16:17]
	v_pk_add_f32 v[66:67], v[66:67], v[18:19]
	global_store_dwordx4 v56, v[64:67], s[10:11]
	v_pk_mul_f32 v[224:225], v[200:201], v[64:65]
	v_pk_mul_f32 v[226:227], v[202:203], v[66:67]
	v_cvt_pk_bf16_f32 v228, v224, v225
	v_cvt_pk_bf16_f32 v229, v226, v227
	global_store_dwordx2 v60, v[228:229], s[28:29]
	v_pk_mul_f32 v[230:231], v[64:65], v[64:65]
	v_pk_mul_f32 v[232:233], v[66:67], v[66:67]
	v_add_f32_e32 v230, v230, v231
	v_add_f32_e32 v230, v232, v230
	v_add_f32_e32 v234, v233, v230
	v_pk_add_f32 v[80:81], v[80:81], v[32:33]
	v_pk_add_f32 v[82:83], v[82:83], v[34:35]
	global_store_dwordx4 v56, v[80:83], s[10:11] offset:64
	v_pk_mul_f32 v[224:225], v[204:205], v[80:81]
	v_pk_mul_f32 v[226:227], v[206:207], v[82:83]
	v_cvt_pk_bf16_f32 v228, v224, v225
	v_cvt_pk_bf16_f32 v229, v226, v227
	global_store_dwordx2 v60, v[228:229], s[28:29] offset:32
	v_pk_mul_f32 v[230:231], v[80:81], v[80:81]
	v_pk_mul_f32 v[232:233], v[82:83], v[82:83]
	v_add_f32_e32 v230, v230, v231
	v_add_f32_e32 v230, v232, v230
	v_add_f32_e32 v230, v233, v230
	v_add_f32_e32 v234, v234, v230
	v_pk_add_f32 v[96:97], v[96:97], v[48:49]
	v_pk_add_f32 v[98:99], v[98:99], v[50:51]
	global_store_dwordx4 v56, v[96:99], s[10:11] offset:128
	v_pk_mul_f32 v[224:225], v[208:209], v[96:97]
	v_pk_mul_f32 v[226:227], v[210:211], v[98:99]
	v_cvt_pk_bf16_f32 v228, v224, v225
	v_cvt_pk_bf16_f32 v229, v226, v227
	global_store_dwordx2 v60, v[228:229], s[28:29] offset:64
	v_pk_mul_f32 v[230:231], v[96:97], v[96:97]
	v_pk_mul_f32 v[232:233], v[98:99], v[98:99]
	v_add_f32_e32 v230, v230, v231
	v_add_f32_e32 v230, v232, v230
	v_add_f32_e32 v230, v233, v230
	v_add_f32_e32 v234, v234, v230
	v_pk_add_f32 v[112:113], v[112:113], v[248:249]
	v_pk_add_f32 v[114:115], v[114:115], v[250:251]
	global_store_dwordx4 v56, v[112:115], s[10:11] offset:192
	v_pk_mul_f32 v[224:225], v[212:213], v[112:113]
	v_pk_mul_f32 v[226:227], v[214:215], v[114:115]
	v_cvt_pk_bf16_f32 v228, v224, v225
	v_cvt_pk_bf16_f32 v229, v226, v227
	global_store_dwordx2 v60, v[228:229], s[28:29] offset:96
	v_pk_mul_f32 v[230:231], v[112:113], v[112:113]
	v_pk_mul_f32 v[232:233], v[114:115], v[114:115]
	v_add_f32_e32 v230, v230, v231
	v_add_f32_e32 v230, v232, v230
	v_add_f32_e32 v235, v233, v230
	v_pk_add_f32 v[128:129], v[128:129], v[168:169]
	v_pk_add_f32 v[130:131], v[130:131], v[170:171]
	global_store_dwordx4 v56, v[128:131], s[10:11] offset:256
	v_pk_mul_f32 v[224:225], v[216:217], v[128:129]
	v_pk_mul_f32 v[226:227], v[218:219], v[130:131]
	v_cvt_pk_bf16_f32 v228, v224, v225
	v_cvt_pk_bf16_f32 v229, v226, v227
	global_store_dwordx2 v60, v[228:229], s[28:29] offset:128
	v_pk_mul_f32 v[230:231], v[128:129], v[128:129]
	v_pk_mul_f32 v[232:233], v[130:131], v[130:131]
	v_add_f32_e32 v230, v230, v231
	v_add_f32_e32 v230, v232, v230
	v_add_f32_e32 v230, v233, v230
	v_add_f32_e32 v235, v235, v230
	v_pk_add_f32 v[144:145], v[144:145], v[184:185]
	v_pk_add_f32 v[146:147], v[146:147], v[186:187]
	global_store_dwordx4 v56, v[144:147], s[10:11] offset:320
	v_pk_mul_f32 v[224:225], v[220:221], v[144:145]
	v_pk_mul_f32 v[226:227], v[222:223], v[146:147]
	v_cvt_pk_bf16_f32 v228, v224, v225
	v_cvt_pk_bf16_f32 v229, v226, v227
	global_store_dwordx2 v60, v[228:229], s[28:29] offset:160
	v_pk_mul_f32 v[230:231], v[144:145], v[144:145]
	v_pk_mul_f32 v[232:233], v[146:147], v[146:147]
	v_add_f32_e32 v230, v230, v231
	v_add_f32_e32 v230, v232, v230
	v_add_f32_e32 v230, v233, v230
	v_add_f32_e32 v235, v235, v230
	ds_bpermute_b32 v236, v13, v234
	ds_bpermute_b32 v237, v13, v235
	s_waitcnt lgkmcnt(0)
	v_add_f32_e32 v234, v234, v236
	v_add_f32_e32 v235, v235, v237
	ds_bpermute_b32 v236, v12, v234
	ds_bpermute_b32 v237, v12, v235
	s_waitcnt lgkmcnt(0)
	v_add_f32_e32 v234, v234, v236
	v_add_f32_e32 v235, v235, v237
	s_and_saveexec_b64 s[2:3], vcc
	global_store_dwordx2 v8, v[234:235], s[26:27]
	s_or_b64 exec, exec, s[2:3]
	v_pk_add_f32 v[68:69], v[68:69], v[20:21]
	v_pk_add_f32 v[70:71], v[70:71], v[22:23]
	global_store_dwordx4 v57, v[68:71], s[10:11]
	v_pk_mul_f32 v[224:225], v[200:201], v[68:69]
	v_pk_mul_f32 v[226:227], v[202:203], v[70:71]
	v_cvt_pk_bf16_f32 v228, v224, v225
	v_cvt_pk_bf16_f32 v229, v226, v227
	global_store_dwordx2 v61, v[228:229], s[28:29]
	v_pk_mul_f32 v[230:231], v[68:69], v[68:69]
	v_pk_mul_f32 v[232:233], v[70:71], v[70:71]
	v_add_f32_e32 v230, v230, v231
	v_add_f32_e32 v230, v232, v230
	v_add_f32_e32 v234, v233, v230
	v_pk_add_f32 v[84:85], v[84:85], v[36:37]
	v_pk_add_f32 v[86:87], v[86:87], v[38:39]
	global_store_dwordx4 v57, v[84:87], s[10:11] offset:64
	v_pk_mul_f32 v[224:225], v[204:205], v[84:85]
	v_pk_mul_f32 v[226:227], v[206:207], v[86:87]
	v_cvt_pk_bf16_f32 v228, v224, v225
	v_cvt_pk_bf16_f32 v229, v226, v227
	global_store_dwordx2 v61, v[228:229], s[28:29] offset:32
	v_pk_mul_f32 v[230:231], v[84:85], v[84:85]
	v_pk_mul_f32 v[232:233], v[86:87], v[86:87]
	v_add_f32_e32 v230, v230, v231
	v_add_f32_e32 v230, v232, v230
	v_add_f32_e32 v230, v233, v230
	v_add_f32_e32 v234, v234, v230
	v_pk_add_f32 v[100:101], v[100:101], v[52:53]
	v_pk_add_f32 v[102:103], v[102:103], v[54:55]
	global_store_dwordx4 v57, v[100:103], s[10:11] offset:128
	v_pk_mul_f32 v[224:225], v[208:209], v[100:101]
	v_pk_mul_f32 v[226:227], v[210:211], v[102:103]
	v_cvt_pk_bf16_f32 v228, v224, v225
	v_cvt_pk_bf16_f32 v229, v226, v227
	global_store_dwordx2 v61, v[228:229], s[28:29] offset:64
	v_pk_mul_f32 v[230:231], v[100:101], v[100:101]
	v_pk_mul_f32 v[232:233], v[102:103], v[102:103]
	v_add_f32_e32 v230, v230, v231
	v_add_f32_e32 v230, v232, v230
	v_add_f32_e32 v230, v233, v230
	v_add_f32_e32 v234, v234, v230
	v_pk_add_f32 v[116:117], v[116:117], v[252:253]
	v_pk_add_f32 v[118:119], v[118:119], v[254:255]
	global_store_dwordx4 v57, v[116:119], s[10:11] offset:192
	v_pk_mul_f32 v[224:225], v[212:213], v[116:117]
	v_pk_mul_f32 v[226:227], v[214:215], v[118:119]
	v_cvt_pk_bf16_f32 v228, v224, v225
	v_cvt_pk_bf16_f32 v229, v226, v227
	global_store_dwordx2 v61, v[228:229], s[28:29] offset:96
	v_pk_mul_f32 v[230:231], v[116:117], v[116:117]
	v_pk_mul_f32 v[232:233], v[118:119], v[118:119]
	v_add_f32_e32 v230, v230, v231
	v_add_f32_e32 v230, v232, v230
	v_add_f32_e32 v235, v233, v230
	v_pk_add_f32 v[132:133], v[132:133], v[172:173]
	v_pk_add_f32 v[134:135], v[134:135], v[174:175]
	global_store_dwordx4 v57, v[132:135], s[10:11] offset:256
	v_pk_mul_f32 v[224:225], v[216:217], v[132:133]
	v_pk_mul_f32 v[226:227], v[218:219], v[134:135]
	v_cvt_pk_bf16_f32 v228, v224, v225
	v_cvt_pk_bf16_f32 v229, v226, v227
	global_store_dwordx2 v61, v[228:229], s[28:29] offset:128
	v_pk_mul_f32 v[230:231], v[132:133], v[132:133]
	v_pk_mul_f32 v[232:233], v[134:135], v[134:135]
	v_add_f32_e32 v230, v230, v231
	v_add_f32_e32 v230, v232, v230
	v_add_f32_e32 v230, v233, v230
	v_add_f32_e32 v235, v235, v230
	v_pk_add_f32 v[148:149], v[148:149], v[188:189]
	v_pk_add_f32 v[150:151], v[150:151], v[190:191]
	global_store_dwordx4 v57, v[148:151], s[10:11] offset:320
	v_pk_mul_f32 v[224:225], v[220:221], v[148:149]
	v_pk_mul_f32 v[226:227], v[222:223], v[150:151]
	v_cvt_pk_bf16_f32 v228, v224, v225
	v_cvt_pk_bf16_f32 v229, v226, v227
	global_store_dwordx2 v61, v[228:229], s[28:29] offset:160
	v_pk_mul_f32 v[230:231], v[148:149], v[148:149]
	v_pk_mul_f32 v[232:233], v[150:151], v[150:151]
	v_add_f32_e32 v230, v230, v231
	v_add_f32_e32 v230, v232, v230
	v_add_f32_e32 v230, v233, v230
	v_add_f32_e32 v235, v235, v230
	ds_bpermute_b32 v236, v13, v234
	ds_bpermute_b32 v237, v13, v235
	s_waitcnt lgkmcnt(0)
	v_add_f32_e32 v234, v234, v236
	v_add_f32_e32 v235, v235, v237
	ds_bpermute_b32 v236, v12, v234
	ds_bpermute_b32 v237, v12, v235
	s_waitcnt lgkmcnt(0)
	v_add_f32_e32 v234, v234, v236
	v_add_f32_e32 v235, v235, v237
	s_and_saveexec_b64 s[2:3], vcc
	global_store_dwordx2 v9, v[234:235], s[26:27]
	s_or_b64 exec, exec, s[2:3]
	v_pk_add_f32 v[72:73], v[72:73], v[24:25]
	v_pk_add_f32 v[74:75], v[74:75], v[26:27]
	global_store_dwordx4 v58, v[72:75], s[10:11]
	v_pk_mul_f32 v[224:225], v[200:201], v[72:73]
	v_pk_mul_f32 v[226:227], v[202:203], v[74:75]
	v_cvt_pk_bf16_f32 v228, v224, v225
	v_cvt_pk_bf16_f32 v229, v226, v227
	global_store_dwordx2 v62, v[228:229], s[28:29]
	v_pk_mul_f32 v[230:231], v[72:73], v[72:73]
	v_pk_mul_f32 v[232:233], v[74:75], v[74:75]
	v_add_f32_e32 v230, v230, v231
	v_add_f32_e32 v230, v232, v230
	v_add_f32_e32 v234, v233, v230
	v_pk_add_f32 v[88:89], v[88:89], v[40:41]
	v_pk_add_f32 v[90:91], v[90:91], v[42:43]
	global_store_dwordx4 v58, v[88:91], s[10:11] offset:64
	v_pk_mul_f32 v[224:225], v[204:205], v[88:89]
	v_pk_mul_f32 v[226:227], v[206:207], v[90:91]
	v_cvt_pk_bf16_f32 v228, v224, v225
	v_cvt_pk_bf16_f32 v229, v226, v227
	global_store_dwordx2 v62, v[228:229], s[28:29] offset:32
	v_pk_mul_f32 v[230:231], v[88:89], v[88:89]
	v_pk_mul_f32 v[232:233], v[90:91], v[90:91]
	v_add_f32_e32 v230, v230, v231
	v_add_f32_e32 v230, v232, v230
	v_add_f32_e32 v230, v233, v230
	v_add_f32_e32 v234, v234, v230
	v_pk_add_f32 v[104:105], v[104:105], v[240:241]
	v_pk_add_f32 v[106:107], v[106:107], v[242:243]
	global_store_dwordx4 v58, v[104:107], s[10:11] offset:128
	v_pk_mul_f32 v[224:225], v[208:209], v[104:105]
	v_pk_mul_f32 v[226:227], v[210:211], v[106:107]
	v_cvt_pk_bf16_f32 v228, v224, v225
	v_cvt_pk_bf16_f32 v229, v226, v227
	global_store_dwordx2 v62, v[228:229], s[28:29] offset:64
	v_pk_mul_f32 v[230:231], v[104:105], v[104:105]
	v_pk_mul_f32 v[232:233], v[106:107], v[106:107]
	v_add_f32_e32 v230, v230, v231
	v_add_f32_e32 v230, v232, v230
	v_add_f32_e32 v230, v233, v230
	v_add_f32_e32 v234, v234, v230
	v_pk_add_f32 v[120:121], v[120:121], v[160:161]
	v_pk_add_f32 v[122:123], v[122:123], v[162:163]
	global_store_dwordx4 v58, v[120:123], s[10:11] offset:192
	v_pk_mul_f32 v[224:225], v[212:213], v[120:121]
	v_pk_mul_f32 v[226:227], v[214:215], v[122:123]
	v_cvt_pk_bf16_f32 v228, v224, v225
	v_cvt_pk_bf16_f32 v229, v226, v227
	global_store_dwordx2 v62, v[228:229], s[28:29] offset:96
	v_pk_mul_f32 v[230:231], v[120:121], v[120:121]
	v_pk_mul_f32 v[232:233], v[122:123], v[122:123]
	v_add_f32_e32 v230, v230, v231
	v_add_f32_e32 v230, v232, v230
	v_add_f32_e32 v235, v233, v230
	v_pk_add_f32 v[136:137], v[136:137], v[176:177]
	v_pk_add_f32 v[138:139], v[138:139], v[178:179]
	global_store_dwordx4 v58, v[136:139], s[10:11] offset:256
	v_pk_mul_f32 v[224:225], v[216:217], v[136:137]
	v_pk_mul_f32 v[226:227], v[218:219], v[138:139]
	v_cvt_pk_bf16_f32 v228, v224, v225
	v_cvt_pk_bf16_f32 v229, v226, v227
	global_store_dwordx2 v62, v[228:229], s[28:29] offset:128
	v_pk_mul_f32 v[230:231], v[136:137], v[136:137]
	v_pk_mul_f32 v[232:233], v[138:139], v[138:139]
	v_add_f32_e32 v230, v230, v231
	v_add_f32_e32 v230, v232, v230
	v_add_f32_e32 v230, v233, v230
	v_add_f32_e32 v235, v235, v230
	v_pk_add_f32 v[152:153], v[152:153], v[192:193]
	v_pk_add_f32 v[154:155], v[154:155], v[194:195]
	global_store_dwordx4 v58, v[152:155], s[10:11] offset:320
	v_pk_mul_f32 v[224:225], v[220:221], v[152:153]
	v_pk_mul_f32 v[226:227], v[222:223], v[154:155]
	v_cvt_pk_bf16_f32 v228, v224, v225
	v_cvt_pk_bf16_f32 v229, v226, v227
	global_store_dwordx2 v62, v[228:229], s[28:29] offset:160
	v_pk_mul_f32 v[230:231], v[152:153], v[152:153]
	v_pk_mul_f32 v[232:233], v[154:155], v[154:155]
	v_add_f32_e32 v230, v230, v231
	v_add_f32_e32 v230, v232, v230
	v_add_f32_e32 v230, v233, v230
	v_add_f32_e32 v235, v235, v230
	ds_bpermute_b32 v236, v13, v234
	ds_bpermute_b32 v237, v13, v235
	s_waitcnt lgkmcnt(0)
	v_add_f32_e32 v234, v234, v236
	v_add_f32_e32 v235, v235, v237
	ds_bpermute_b32 v236, v12, v234
	ds_bpermute_b32 v237, v12, v235
	s_waitcnt lgkmcnt(0)
	v_add_f32_e32 v234, v234, v236
	v_add_f32_e32 v235, v235, v237
	s_and_saveexec_b64 s[2:3], vcc
	global_store_dwordx2 v10, v[234:235], s[26:27]
	s_or_b64 exec, exec, s[2:3]
	v_pk_add_f32 v[76:77], v[76:77], v[28:29]
	v_pk_add_f32 v[78:79], v[78:79], v[30:31]
	global_store_dwordx4 v59, v[76:79], s[10:11]
	v_pk_mul_f32 v[224:225], v[200:201], v[76:77]
	v_pk_mul_f32 v[226:227], v[202:203], v[78:79]
	v_cvt_pk_bf16_f32 v228, v224, v225
	v_cvt_pk_bf16_f32 v229, v226, v227
	global_store_dwordx2 v63, v[228:229], s[28:29]
	v_pk_mul_f32 v[230:231], v[76:77], v[76:77]
	v_pk_mul_f32 v[232:233], v[78:79], v[78:79]
	v_add_f32_e32 v230, v230, v231
	v_add_f32_e32 v230, v232, v230
	v_add_f32_e32 v234, v233, v230
	v_pk_add_f32 v[92:93], v[92:93], v[44:45]
	v_pk_add_f32 v[94:95], v[94:95], v[46:47]
	global_store_dwordx4 v59, v[92:95], s[10:11] offset:64
	v_pk_mul_f32 v[224:225], v[204:205], v[92:93]
	v_pk_mul_f32 v[226:227], v[206:207], v[94:95]
	v_cvt_pk_bf16_f32 v228, v224, v225
	v_cvt_pk_bf16_f32 v229, v226, v227
	global_store_dwordx2 v63, v[228:229], s[28:29] offset:32
	v_pk_mul_f32 v[230:231], v[92:93], v[92:93]
	v_pk_mul_f32 v[232:233], v[94:95], v[94:95]
	v_add_f32_e32 v230, v230, v231
	v_add_f32_e32 v230, v232, v230
	v_add_f32_e32 v230, v233, v230
	v_add_f32_e32 v234, v234, v230
	v_pk_add_f32 v[108:109], v[108:109], v[244:245]
	v_pk_add_f32 v[110:111], v[110:111], v[246:247]
	global_store_dwordx4 v59, v[108:111], s[10:11] offset:128
	v_pk_mul_f32 v[224:225], v[208:209], v[108:109]
	v_pk_mul_f32 v[226:227], v[210:211], v[110:111]
	v_cvt_pk_bf16_f32 v228, v224, v225
	v_cvt_pk_bf16_f32 v229, v226, v227
	global_store_dwordx2 v63, v[228:229], s[28:29] offset:64
	v_pk_mul_f32 v[230:231], v[108:109], v[108:109]
	v_pk_mul_f32 v[232:233], v[110:111], v[110:111]
	v_add_f32_e32 v230, v230, v231
	v_add_f32_e32 v230, v232, v230
	v_add_f32_e32 v230, v233, v230
	v_add_f32_e32 v234, v234, v230
	v_pk_add_f32 v[124:125], v[124:125], v[164:165]
	v_pk_add_f32 v[126:127], v[126:127], v[166:167]
	global_store_dwordx4 v59, v[124:127], s[10:11] offset:192
	v_pk_mul_f32 v[224:225], v[212:213], v[124:125]
	v_pk_mul_f32 v[226:227], v[214:215], v[126:127]
	v_cvt_pk_bf16_f32 v228, v224, v225
	v_cvt_pk_bf16_f32 v229, v226, v227
	global_store_dwordx2 v63, v[228:229], s[28:29] offset:96
	v_pk_mul_f32 v[230:231], v[124:125], v[124:125]
	v_pk_mul_f32 v[232:233], v[126:127], v[126:127]
	v_add_f32_e32 v230, v230, v231
	v_add_f32_e32 v230, v232, v230
	v_add_f32_e32 v235, v233, v230
	v_pk_add_f32 v[140:141], v[140:141], v[180:181]
	v_pk_add_f32 v[142:143], v[142:143], v[182:183]
	global_store_dwordx4 v59, v[140:143], s[10:11] offset:256
	v_pk_mul_f32 v[224:225], v[216:217], v[140:141]
	v_pk_mul_f32 v[226:227], v[218:219], v[142:143]
	v_cvt_pk_bf16_f32 v228, v224, v225
	v_cvt_pk_bf16_f32 v229, v226, v227
	global_store_dwordx2 v63, v[228:229], s[28:29] offset:128
	v_pk_mul_f32 v[230:231], v[140:141], v[140:141]
	v_pk_mul_f32 v[232:233], v[142:143], v[142:143]
	v_add_f32_e32 v230, v230, v231
	v_add_f32_e32 v230, v232, v230
	v_add_f32_e32 v230, v233, v230
	v_add_f32_e32 v235, v235, v230
	v_pk_add_f32 v[156:157], v[156:157], v[196:197]
	v_pk_add_f32 v[158:159], v[158:159], v[198:199]
	global_store_dwordx4 v59, v[156:159], s[10:11] offset:320
	v_pk_mul_f32 v[224:225], v[220:221], v[156:157]
	v_pk_mul_f32 v[226:227], v[222:223], v[158:159]
	v_cvt_pk_bf16_f32 v228, v224, v225
	v_cvt_pk_bf16_f32 v229, v226, v227
	global_store_dwordx2 v63, v[228:229], s[28:29] offset:160
	v_pk_mul_f32 v[230:231], v[156:157], v[156:157]
	v_pk_mul_f32 v[232:233], v[158:159], v[158:159]
	v_add_f32_e32 v230, v230, v231
	v_add_f32_e32 v230, v232, v230
	v_add_f32_e32 v230, v233, v230
	v_add_f32_e32 v235, v235, v230
	ds_bpermute_b32 v236, v13, v234
	ds_bpermute_b32 v237, v13, v235
	s_waitcnt lgkmcnt(0)
	v_add_f32_e32 v234, v234, v236
	v_add_f32_e32 v235, v235, v237
	ds_bpermute_b32 v236, v12, v234
	ds_bpermute_b32 v237, v12, v235
	s_waitcnt lgkmcnt(0)
	v_add_f32_e32 v234, v234, v236
	v_add_f32_e32 v235, v235, v237
	s_and_saveexec_b64 s[2:3], vcc
	global_store_dwordx2 v11, v[234:235], s[26:27]
	s_or_b64 exec, exec, s[2:3]

	.amdhsa_kernel _Z7gemm128ILi1ELi96EEv8GemmArgs
		.amdhsa_group_segment_fixed_size 98304
		.amdhsa_private_segment_fixed_size 0
		.amdhsa_kernarg_size 80
		.amdhsa_user_sgpr_count 2
		.amdhsa_user_sgpr_dispatch_ptr 0
		.amdhsa_user_sgpr_queue_ptr 0
		.amdhsa_user_sgpr_kernarg_segment_ptr 1
		.amdhsa_user_sgpr_dispatch_id 0
		.amdhsa_user_sgpr_kernarg_preload_length 0
		.amdhsa_user_sgpr_kernarg_preload_offset 0
		.amdhsa_user_sgpr_private_segment_size 0
		.amdhsa_uses_dynamic_stack 0
		.amdhsa_enable_private_segment 0
		.amdhsa_system_sgpr_workgroup_id_x 1
		.amdhsa_system_sgpr_workgroup_id_y 0
		.amdhsa_system_sgpr_workgroup_id_z 0
		.amdhsa_system_sgpr_workgroup_info 0
		.amdhsa_system_vgpr_workitem_id 0
		.amdhsa_next_free_vgpr 256
		.amdhsa_next_free_sgpr 31
		.amdhsa_accum_offset 256
		.amdhsa_reserve_vcc 1
		.amdhsa_float_round_mode_32 0
		.amdhsa_float_round_mode_16_64 0
		.amdhsa_float_denorm_mode_32 3
		.amdhsa_float_denorm_mode_16_64 3
		.amdhsa_dx10_clamp 1
		.amdhsa_ieee_mode 1
		.amdhsa_fp16_overflow 0
		.amdhsa_tg_split 0
		.amdhsa_exception_fp_ieee_invalid_op 0
		.amdhsa_exception_fp_denorm_src 0
		.amdhsa_exception_fp_ieee_div_zero 0
		.amdhsa_exception_fp_ieee_overflow 0
		.amdhsa_exception_fp_ieee_underflow 0
		.amdhsa_exception_fp_ieee_inexact 0
		.amdhsa_exception_int_div_zero 0
	.end_amdhsa_kernel

.Lfunc_end2:
	.size	_Z7gemm128ILi1ELi96EEv8GemmArgs, .Lfunc_end2-_Z7gemm128ILi1ELi96EEv8GemmArgs
	.set _Z7gemm128ILi1ELi96EEv8GemmArgs.num_vgpr, 256
	.set _Z7gemm128ILi1ELi96EEv8GemmArgs.num_agpr, 0
	.set _Z7gemm128ILi1ELi96EEv8GemmArgs.numbered_sgpr, 31
	.set _Z7gemm128ILi1ELi96EEv8GemmArgs.num_named_barrier, 0
	.set _Z7gemm128ILi1ELi96EEv8GemmArgs.private_seg_size, 0
	.set _Z7gemm128ILi1ELi96EEv8GemmArgs.uses_vcc, 1
	.set _Z7gemm128ILi1ELi96EEv8GemmArgs.uses_flat_scratch, 0
	.set _Z7gemm128ILi1ELi96EEv8GemmArgs.has_dyn_sized_stack, 0
	.set _Z7gemm128ILi1ELi96EEv8GemmArgs.has_recursion, 0
	.set _Z7gemm128ILi1ELi96EEv8GemmArgs.has_indirect_call, 0

amdhsa.kernels:
  - .agpr_count:     0
    .args:
      - .offset:         0
        .size:           136
        .value_kind:     by_value
      - .offset:         136
        .size:           4
        .value_kind:     hidden_block_count_x
      - .offset:         140
        .size:           4
        .value_kind:     hidden_block_count_y
      - .offset:         144
        .size:           4
        .value_kind:     hidden_block_count_z
      - .offset:         148
        .size:           2
        .value_kind:     hidden_group_size_x
      - .offset:         150
        .size:           2
        .value_kind:     hidden_group_size_y
      - .offset:         152
        .size:           2
        .value_kind:     hidden_group_size_z
      - .offset:         154
        .size:           2
        .value_kind:     hidden_remainder_x
      - .offset:         156
        .size:           2
        .value_kind:     hidden_remainder_y
      - .offset:         158
        .size:           2
        .value_kind:     hidden_remainder_z
      - .offset:         176
        .size:           8
        .value_kind:     hidden_global_offset_x
      - .offset:         184
        .size:           8
        .value_kind:     hidden_global_offset_y
      - .offset:         192
        .size:           8
        .value_kind:     hidden_global_offset_z
      - .offset:         200
        .size:           2
        .value_kind:     hidden_grid_dims
    .group_segment_fixed_size: 16640
    .kernarg_segment_align: 8
    .kernarg_segment_size: 392
    .language:       OpenCL C
    .language_version:
      - 2
      - 0
    .max_flat_workgroup_size: 256
    .name:           _Z11prep_kernel8PrepArgs
    .private_segment_fixed_size: 0
    .sgpr_count:     26
    .sgpr_spill_count: 0
    .symbol:         _Z11prep_kernel8PrepArgs.kd
    .uniform_work_group_size: 1
    .uses_dynamic_stack: false
    .vgpr_count:     46
    .vgpr_spill_count: 0
    .wavefront_size: 64
  - .agpr_count:     0
    .args:
      - .offset:         0
        .size:           216
        .value_kind:     by_value
    .group_segment_fixed_size: 0
    .kernarg_segment_align: 8
    .kernarg_segment_size: 216
    .language:       OpenCL C
    .language_version:
      - 2
      - 0
    .max_flat_workgroup_size: 512
    .name:           _Z11attn_kernel8AttnArgs
    .private_segment_fixed_size: 0
    .sgpr_count:     82
    .sgpr_spill_count: 0
    .symbol:         _Z11attn_kernel8AttnArgs.kd
    .uniform_work_group_size: 1
    .uses_dynamic_stack: false
    .vgpr_count:     220
    .vgpr_spill_count: 0
    .wavefront_size: 64
  - .agpr_count:     0
    .args:
      - .offset:         0
        .size:           80
        .value_kind:     by_value
    .group_segment_fixed_size: 98304
    .kernarg_segment_align: 8
    .kernarg_segment_size: 80
    .language:       OpenCL C
    .language_version:
      - 2
      - 0
    .max_flat_workgroup_size: 256
    .name:           _Z7gemm128ILi1ELi96EEv8GemmArgs
    .private_segment_fixed_size: 0
    .sgpr_count:     37
    .sgpr_spill_count: 0
    .symbol:         _Z7gemm128ILi1ELi96EEv8GemmArgs.kd
    .uniform_work_group_size: 1
    .uses_dynamic_stack: false
    .vgpr_count:     256
    .vgpr_spill_count: 0
    .wavefront_size: 64
  - .agpr_count:     0
    .args:
      - .offset:         0
        .size:           80
        .value_kind:     by_value
    .group_segment_fixed_size: 0
    .kernarg_segment_align: 8
    .kernarg_segment_size: 80
    .language:       OpenCL C
    .language_version:
      - 2
      - 0
    .max_flat_workgroup_size: 256
    .name:           _Z7gemm128ILi2ELi128EEv8GemmArgs
    .private_segment_fixed_size: 0
    .sgpr_count:     22
    .sgpr_spill_count: 0
    .symbol:         _Z7gemm128ILi2ELi128EEv8GemmArgs.kd
    .uniform_work_group_size: 1
    .uses_dynamic_stack: false
    .vgpr_count:     166
    .vgpr_spill_count: 0
    .wavefront_size: 64
  - .agpr_count:     0
    .args:
      - .offset:         0
        .size:           80
        .value_kind:     by_value
    .group_segment_fixed_size: 98304
    .kernarg_segment_align: 8
    .kernarg_segment_size: 80
    .language:       OpenCL C
    .language_version:
      - 2
      - 0
    .max_flat_workgroup_size: 256
    .name:           _Z7gemm128ILi3ELi96EEv8GemmArgs
    .private_segment_fixed_size: 0
    .sgpr_count:     30
    .sgpr_spill_count: 0
    .symbol:         _Z7gemm128ILi3ELi96EEv8GemmArgs.kd
    .uniform_work_group_size: 1
    .uses_dynamic_stack: false
    .vgpr_count:     256
    .vgpr_spill_count: 0
    .wavefront_size: 64
  - .agpr_count:     0
    .args:
      - .offset:         0
        .size:           32
        .value_kind:     by_value
      - .offset:         32
        .size:           56
        .value_kind:     by_value
    .group_segment_fixed_size: 0
    .kernarg_segment_align: 8
    .kernarg_segment_size: 88
    .language:       OpenCL C
    .language_version:
      - 2
      - 0
    .max_flat_workgroup_size: 512
    .name:           _Z8gemm_bigIN3pg86EpiQKVEEvNS0_4GemmET_
    .private_segment_fixed_size: 0
    .sgpr_count:     58
    .sgpr_spill_count: 0
    .symbol:         _Z8gemm_bigIN3pg86EpiQKVEEvNS0_4GemmET_.kd
    .uniform_work_group_size: 1
    .uses_dynamic_stack: false
    .vgpr_count:     228
    .vgpr_spill_count: 0
    .wavefront_size: 64
  - .agpr_count:     0
    .args:
      - .offset:         0
        .size:           32
        .value_kind:     by_value
      - .offset:         32
        .size:           32
        .value_kind:     by_value
    .group_segment_fixed_size: 0
    .kernarg_segment_align: 8
    .kernarg_segment_size: 64
    .language:       OpenCL C
    .language_version:
      - 2
      - 0
    .max_flat_workgroup_size: 512
    .name:           _Z8gemm_bigIN3pg85EpiUPEEvNS0_4GemmET_
    .private_segment_fixed_size: 0
    .sgpr_count:     50
    .sgpr_spill_count: 0
    .symbol:         _Z8gemm_bigIN3pg85EpiUPEEvNS0_4GemmET_.kd
    .uniform_work_group_size: 1
    .uses_dynamic_stack: false
    .vgpr_count:     226
    .vgpr_spill_count: 0
    .wavefront_size: 64
